# main: one static s_setprio 1 for waves 0-3 (older half) at kernel entry
# speedup vs baseline: 1.0180x; 1.0180x over previous
_Z7na_mainPKDF16_PKhS0_PKfS4_S4_S4_Pf:
	v_readfirstlane_b32 s36, v0
	s_nop 3
	s_lshr_b32 s36, s36, 6
	s_cmp_lt_u32 s36, 4
	s_cbranch_scc0 .Lprio_done
	s_setprio 1
